# P2 background converter paced every attention tile step (was every 2) now that P2 carries 17408 items
# baseline (speedup 1.0000x reference)
;     __device__ __forceinline__ CvtDesc desc(int qq) const { return cvt_desc(*F, item_of(qq), qq & 1, h); }
;     __device__ __forceinline__ void tick() { flush(); if (state == 2) { proc(); state = 0; } else if (state == 1) state = 2; }
; template <int D, bool MASK, bool BIAS, bool SINK, bool REV, bool O8, class BG>
; __device__ __forceinline__ void attn_unit(const Prm& P, LAS unsigned char* lds, BG& bg) {
;     ...
;         bg.tick();
;         if (more) dma_tile(REV ? t - 1 : t + 1, s ^ 1);
;         bg.issue();
;     __device__ __forceinline__ void proc() { cvt_to_lds(buf, desc(q), img, gl, q & 1, h, F->lane); if (q & 1) fitem = item_of(q); ++q; }
.LBB0_465:
	s_lshl_b32 s24, s38, 7
	s_lshl_b32 s11, s60, 7
	s_lshl_b32 s38, s62, 5
	s_and_b32 s11, s11, 0x780
	s_and_b32 s38, s38, 32
	s_or_b32 s11, s38, s11
	v_or_b32_e32 v2, s11, v201
	v_mul_u32_u24_e32 v2, s96, v2
	v_lshlrev_b32_e32 v2, 2, v2
	v_lshl_add_u64 v[36:37], s[6:7], 0, v[2:3]
	v_lshl_add_u64 v[36:37], s[24:25], 2, v[36:37]
	v_mov_b32_e32 v185, v3
	v_lshl_add_u64 v[36:37], v[36:37], 0, v[184:185]
	s_lshl_b32 s24, s96, 2
	v_lshl_add_u64 v[38:39], v[36:37], 0, s[24:25]
	global_load_dwordx4 v[108:111], v[36:37], off nt
	global_load_dwordx4 v[104:107], v[38:39], off nt
	v_lshl_add_u64 v[36:37], v[38:39], 0, s[24:25]
	v_lshl_add_u64 v[38:39], v[36:37], 0, s[24:25]
	global_load_dwordx4 v[156:159], v[36:37], off nt
	global_load_dwordx4 v[144:147], v[38:39], off nt
	v_lshl_add_u64 v[36:37], v[38:39], 0, s[24:25]
	v_lshl_add_u64 v[38:39], v[36:37], 0, s[24:25]
	global_load_dwordx4 v[152:155], v[36:37], off nt
	global_load_dwordx4 v[140:143], v[38:39], off nt
	v_lshl_add_u64 v[36:37], v[38:39], 0, s[24:25]
	v_lshl_add_u64 v[38:39], v[36:37], 0, s[24:25]
	global_load_dwordx4 v[136:139], v[36:37], off nt
	global_load_dwordx4 v[128:131], v[38:39], off nt
	v_lshl_add_u64 v[36:37], v[38:39], 0, s[24:25]
	global_load_dwordx4 v[116:119], v[36:37], off nt
	v_lshl_add_u64 v[36:37], v[36:37], 0, s[24:25]
	global_load_dwordx4 v[124:127], v[36:37], off nt
	v_lshl_add_u64 v[36:37], v[36:37], 0, s[24:25]
	global_load_dwordx4 v[132:135], v[36:37], off nt
	v_lshl_add_u64 v[36:37], v[36:37], 0, s[24:25]
	global_load_dwordx4 v[148:151], v[36:37], off nt
	v_lshl_add_u64 v[36:37], v[36:37], 0, s[24:25]
	global_load_dwordx4 v[112:115], v[36:37], off nt
	v_lshl_add_u64 v[36:37], v[36:37], 0, s[24:25]
	global_load_dwordx4 v[120:123], v[36:37], off nt
	v_lshl_add_u64 v[36:37], v[36:37], 0, s[24:25]
	global_load_dwordx4 v[96:99], v[36:37], off nt
	v_lshl_add_u64 v[36:37], v[36:37], 0, s[24:25]
	global_load_dwordx4 v[100:103], v[36:37], off nt
	s_mov_b32 s60, 1
	s_mov_b32 s38, 1

;     __device__ __forceinline__ CvtDesc desc(int qq) const { return cvt_desc(*F, item_of(qq), qq & 1, h); }
;     __device__ __forceinline__ void tick() { flush(); if (state == 2) { proc(); state = 0; } else if (state == 1) state = 2; }
; template <int D, bool MASK, bool BIAS, bool SINK, bool REV, bool O8, class BG>
; __device__ __forceinline__ void attn_unit(const Prm& P, LAS unsigned char* lds, BG& bg) {
;     ...
;         bg.tick();
;         if (more) dma_tile(REV ? t - 1 : t + 1, s ^ 1);
;         bg.issue();
;     __device__ __forceinline__ void proc() { cvt_to_lds(buf, desc(q), img, gl, q & 1, h, F->lane); if (q & 1) fitem = item_of(q); ++q; }
.LBB0_602:
	s_lshl_b32 s14, s38, 7
	s_lshl_b32 s11, s11, 7
	s_lshl_b32 s38, s10, 5
	s_and_b32 s11, s11, 0x780
	s_and_b32 s38, s38, 32
	s_or_b32 s11, s38, s11
	v_or_b32_e32 v34, s11, v171
	v_mul_u32_u24_e32 v34, s80, v34
	v_lshlrev_b32_e32 v82, 2, v34
	v_lshl_add_u64 v[34:35], s[6:7], 0, v[82:83]
	v_lshl_add_u64 v[34:35], s[14:15], 2, v[34:35]
	v_mov_b32_e32 v91, v83
	v_lshl_add_u64 v[34:35], v[34:35], 0, v[90:91]
	s_lshl_b32 s14, s80, 2
	v_lshl_add_u64 v[36:37], v[34:35], 0, s[14:15]
	global_load_dwordx4 v[108:111], v[34:35], off nt
	global_load_dwordx4 v[104:107], v[36:37], off nt
	v_lshl_add_u64 v[34:35], v[36:37], 0, s[14:15]
	v_lshl_add_u64 v[36:37], v[34:35], 0, s[14:15]
	global_load_dwordx4 v[156:159], v[34:35], off nt
	global_load_dwordx4 v[144:147], v[36:37], off nt
	v_lshl_add_u64 v[34:35], v[36:37], 0, s[14:15]
	v_lshl_add_u64 v[36:37], v[34:35], 0, s[14:15]
	global_load_dwordx4 v[152:155], v[34:35], off nt
	global_load_dwordx4 v[140:143], v[36:37], off nt
	v_lshl_add_u64 v[34:35], v[36:37], 0, s[14:15]
	v_lshl_add_u64 v[36:37], v[34:35], 0, s[14:15]
	global_load_dwordx4 v[136:139], v[34:35], off nt
	global_load_dwordx4 v[128:131], v[36:37], off nt
	v_lshl_add_u64 v[34:35], v[36:37], 0, s[14:15]
	global_load_dwordx4 v[116:119], v[34:35], off nt
	v_lshl_add_u64 v[34:35], v[34:35], 0, s[14:15]
	global_load_dwordx4 v[124:127], v[34:35], off nt
	v_lshl_add_u64 v[34:35], v[34:35], 0, s[14:15]
	global_load_dwordx4 v[132:135], v[34:35], off nt
	v_lshl_add_u64 v[34:35], v[34:35], 0, s[14:15]
	global_load_dwordx4 v[148:151], v[34:35], off nt
	v_lshl_add_u64 v[34:35], v[34:35], 0, s[14:15]
	global_load_dwordx4 v[112:115], v[34:35], off nt
	v_lshl_add_u64 v[34:35], v[34:35], 0, s[14:15]
	global_load_dwordx4 v[120:123], v[34:35], off nt
	v_lshl_add_u64 v[34:35], v[34:35], 0, s[14:15]
	global_load_dwordx4 v[96:99], v[34:35], off nt
	v_lshl_add_u64 v[34:35], v[34:35], 0, s[14:15]
	global_load_dwordx4 v[100:103], v[34:35], off nt
	s_mov_b32 s60, 1
	s_mov_b32 s38, 1
